# baseline (speedup 1.0000x reference)
.LBB2_24:
	s_or_b64 exec, exec, s[0:1]
	s_waitcnt lgkmcnt(0)
	ds_read_b128 v[142:145], v130 offset:0
	ds_read_b128 v[146:149], v130 offset:1024
	ds_read_b128 v[150:153], v130 offset:2048
	s_lshl_b32 s0, s33, 8
	s_lshl_b32 s1, s52, 5
	s_or_b32 s4, s0, s1
	s_mul_i32 s0, s4, 0x600
	s_mul_hi_i32 s1, s4, 0x600
	s_add_u32 s0, s42, s0
	s_addc_u32 s1, s43, s1
	s_xor_b32 s2, s4, 0xe0
	s_mul_hi_i32 s3, s2, 0x600
	s_mulk_i32 s2, 0x600
	s_add_u32 s2, s42, s2
	s_addc_u32 s3, s43, s3
	v_lshlrev_b32_e32 v134, 2, v140
	v_lshl_or_b32 v134, v133, 7, v134
	v_mul_u32_u24_e32 v136, 0x1800, v139
	v_add_u32_e32 v136, v136, v134
	v_add_u32_e32 v136, 0xc00, v136
	v_add_u32_e32 v137, 0x3000, v136
	v_add_u32_e32 v138, 0x6000, v136
	v_add_u32_e32 v141, 0x9000, v136
	ds_read_b128 v[154:157], v130 offset:3072
	s_waitcnt vmcnt(15) lgkmcnt(3)
	v_mfma_f32_32x32x16_f16 v[16:31], v[142:145], v[94:97], 0
	ds_read_b128 v[142:145], v130 offset:4096
	s_waitcnt vmcnt(14) lgkmcnt(3)
	v_mfma_f32_32x32x16_f16 v[16:31], v[146:149], v[90:93], v[16:31]
	ds_read_b128 v[146:149], v130 offset:5120
	s_waitcnt vmcnt(13) lgkmcnt(3)
	v_mfma_f32_32x32x16_f16 v[16:31], v[150:153], v[86:89], v[16:31]
	ds_read_b128 v[150:153], v130 offset:6144
	s_waitcnt vmcnt(12) lgkmcnt(3)
	v_mfma_f32_32x32x16_f16 v[16:31], v[154:157], v[82:85], v[16:31]
	ds_read_b128 v[154:157], v130 offset:7168
	s_waitcnt vmcnt(11) lgkmcnt(3)
	v_mfma_f32_32x32x16_f16 v[16:31], v[142:145], v[78:81], v[16:31]
	ds_read_b128 v[142:145], v130 offset:8192
	s_waitcnt vmcnt(10) lgkmcnt(3)
	v_mfma_f32_32x32x16_f16 v[16:31], v[146:149], v[74:77], v[16:31]
	ds_read_b128 v[146:149], v130 offset:9216
	s_waitcnt vmcnt(9) lgkmcnt(3)
	v_mfma_f32_32x32x16_f16 v[16:31], v[150:153], v[70:73], v[16:31]
	ds_read_b128 v[150:153], v130 offset:10240
	s_waitcnt vmcnt(8) lgkmcnt(3)
	v_mfma_f32_32x32x16_f16 v[16:31], v[154:157], v[66:69], v[16:31]
	ds_read_b128 v[154:157], v130 offset:11264
	s_waitcnt vmcnt(7) lgkmcnt(3)
	v_mfma_f32_32x32x16_f16 v[16:31], v[142:145], v[62:65], v[16:31]
	ds_read_b128 v[142:145], v130 offset:12288
	s_waitcnt vmcnt(6) lgkmcnt(3)
	v_mfma_f32_32x32x16_f16 v[16:31], v[146:149], v[58:61], v[16:31]
	ds_read_b128 v[146:149], v130 offset:13312
	s_waitcnt vmcnt(5) lgkmcnt(3)
	v_mfma_f32_32x32x16_f16 v[16:31], v[150:153], v[54:57], v[16:31]
	ds_read_b128 v[150:153], v130 offset:14336
	s_waitcnt vmcnt(4) lgkmcnt(3)
	v_mfma_f32_32x32x16_f16 v[16:31], v[154:157], v[50:53], v[16:31]
	ds_read_b128 v[154:157], v130 offset:15360
	s_waitcnt vmcnt(3) lgkmcnt(3)
	v_mfma_f32_32x32x16_f16 v[16:31], v[142:145], v[46:49], v[16:31]
	ds_read_b128 v[142:145], v130 offset:16384
	s_waitcnt vmcnt(2) lgkmcnt(3)
	v_mfma_f32_32x32x16_f16 v[16:31], v[146:149], v[42:45], v[16:31]
	ds_read_b128 v[146:149], v130 offset:17408
	s_waitcnt vmcnt(1) lgkmcnt(3)
	v_mfma_f32_32x32x16_f16 v[16:31], v[150:153], v[38:41], v[16:31]
	ds_read_b128 v[150:153], v130 offset:18432
	s_waitcnt vmcnt(0) lgkmcnt(3)
	v_mfma_f32_32x32x16_f16 v[16:31], v[154:157], v[34:37], v[16:31]
	global_load_dword v135, v134, s[40:41]
	ds_read_b128 v[154:157], v130 offset:19456
	s_waitcnt lgkmcnt(3)
	v_mfma_f32_32x32x16_f16 v[16:31], v[142:145], v[126:129], v[16:31]
	ds_read_b128 v[142:145], v130 offset:20480
	s_waitcnt lgkmcnt(3)
	v_mfma_f32_32x32x16_f16 v[16:31], v[146:149], v[122:125], v[16:31]
	ds_read_b128 v[146:149], v130 offset:21504
	s_waitcnt lgkmcnt(3)
	v_mfma_f32_32x32x16_f16 v[16:31], v[150:153], v[118:121], v[16:31]
	ds_read_b128 v[150:153], v130 offset:22528
	s_waitcnt lgkmcnt(3)
	v_mfma_f32_32x32x16_f16 v[16:31], v[154:157], v[110:113], v[16:31]
	ds_read_b128 v[154:157], v130 offset:23552
	s_waitcnt lgkmcnt(3)
	v_mfma_f32_32x32x16_f16 v[16:31], v[142:145], v[114:117], v[16:31]
	s_waitcnt lgkmcnt(2)
	v_mfma_f32_32x32x16_f16 v[16:31], v[146:149], v[106:109], v[16:31]
	s_waitcnt lgkmcnt(1)
	v_mfma_f32_32x32x16_f16 v[16:31], v[150:153], v[102:105], v[16:31]
	s_waitcnt lgkmcnt(0)
	v_mfma_f32_32x32x16_f16 v[16:31], v[154:157], v[98:101], v[16:31]
	s_waitcnt lgkmcnt(0)
	s_barrier
	ds_read_b128 v[142:145], v130 offset:24576
	ds_read_b128 v[146:149], v130 offset:25600
	ds_read_b128 v[150:153], v130 offset:26624
	ds_read_b128 v[154:157], v130 offset:27648
	s_waitcnt lgkmcnt(3)
	v_mfma_f32_32x32x16_f16 v[0:15], v[142:145], v[94:97], 0
	ds_read_b128 v[142:145], v130 offset:28672
	s_waitcnt lgkmcnt(3)
	v_mfma_f32_32x32x16_f16 v[0:15], v[146:149], v[90:93], v[0:15]
	ds_read_b128 v[146:149], v130 offset:29696
	s_waitcnt lgkmcnt(3)
	v_mfma_f32_32x32x16_f16 v[0:15], v[150:153], v[86:89], v[0:15]
	ds_read_b128 v[150:153], v130 offset:30720
	s_waitcnt lgkmcnt(3)
	v_mfma_f32_32x32x16_f16 v[0:15], v[154:157], v[82:85], v[0:15]
	s_waitcnt vmcnt(0)
	ds_read_b128 v[154:157], v130 offset:31744
	s_waitcnt lgkmcnt(3)
	v_mfma_f32_32x32x16_f16 v[0:15], v[142:145], v[78:81], v[0:15]
	v_add_f32_e32 v16, v135, v16
	global_store_dword v136, v16, s[0:1] offset:-3072 nt
	ds_read_b128 v[142:145], v130 offset:32768
	s_waitcnt lgkmcnt(3)
	v_mfma_f32_32x32x16_f16 v[0:15], v[146:149], v[74:77], v[0:15]
	v_add_f32_e32 v17, v135, v17
	global_store_dword v136, v17, s[0:1] offset:-1536 nt
	ds_read_b128 v[146:149], v130 offset:33792
	s_waitcnt lgkmcnt(3)
	v_mfma_f32_32x32x16_f16 v[0:15], v[150:153], v[70:73], v[0:15]
	v_add_f32_e32 v18, v135, v18
	global_store_dword v136, v18, s[0:1] offset:0 nt
	ds_read_b128 v[150:153], v130 offset:34816
	s_waitcnt lgkmcnt(3)
	v_mfma_f32_32x32x16_f16 v[0:15], v[154:157], v[66:69], v[0:15]
	v_add_f32_e32 v19, v135, v19
	global_store_dword v136, v19, s[0:1] offset:1536 nt
	ds_read_b128 v[154:157], v130 offset:35840
	s_waitcnt lgkmcnt(3)
	v_mfma_f32_32x32x16_f16 v[0:15], v[142:145], v[62:65], v[0:15]
	v_add_f32_e32 v20, v135, v20
	global_store_dword v137, v20, s[0:1] offset:-3072 nt
	ds_read_b128 v[142:145], v130 offset:36864
	s_waitcnt lgkmcnt(3)
	v_mfma_f32_32x32x16_f16 v[0:15], v[146:149], v[58:61], v[0:15]
	v_add_f32_e32 v21, v135, v21
	global_store_dword v137, v21, s[0:1] offset:-1536 nt
	ds_read_b128 v[146:149], v130 offset:37888
	s_waitcnt lgkmcnt(3)
	v_mfma_f32_32x32x16_f16 v[0:15], v[150:153], v[54:57], v[0:15]
	v_add_f32_e32 v22, v135, v22
	global_store_dword v137, v22, s[0:1] offset:0 nt
	ds_read_b128 v[150:153], v130 offset:38912
	s_waitcnt lgkmcnt(3)
	v_mfma_f32_32x32x16_f16 v[0:15], v[154:157], v[50:53], v[0:15]
	v_add_f32_e32 v23, v135, v23
	global_store_dword v137, v23, s[0:1] offset:1536 nt
	ds_read_b128 v[154:157], v130 offset:39936
	s_waitcnt lgkmcnt(3)
	v_mfma_f32_32x32x16_f16 v[0:15], v[142:145], v[46:49], v[0:15]
	v_add_f32_e32 v24, v135, v24
	global_store_dword v138, v24, s[0:1] offset:-3072 nt
	ds_read_b128 v[142:145], v130 offset:40960
	s_waitcnt lgkmcnt(3)
	v_mfma_f32_32x32x16_f16 v[0:15], v[146:149], v[42:45], v[0:15]
	v_add_f32_e32 v25, v135, v25
	global_store_dword v138, v25, s[0:1] offset:-1536 nt
	ds_read_b128 v[146:149], v130 offset:41984
	s_waitcnt lgkmcnt(3)
	v_mfma_f32_32x32x16_f16 v[0:15], v[150:153], v[38:41], v[0:15]
	v_add_f32_e32 v26, v135, v26
	global_store_dword v138, v26, s[0:1] offset:0 nt
	ds_read_b128 v[150:153], v130 offset:43008
	s_waitcnt lgkmcnt(3)
	v_mfma_f32_32x32x16_f16 v[0:15], v[154:157], v[34:37], v[0:15]
	v_add_f32_e32 v27, v135, v27
	global_store_dword v138, v27, s[0:1] offset:1536 nt
	ds_read_b128 v[154:157], v130 offset:44032
	s_waitcnt lgkmcnt(3)
	v_mfma_f32_32x32x16_f16 v[0:15], v[142:145], v[126:129], v[0:15]
	v_add_f32_e32 v28, v135, v28
	global_store_dword v141, v28, s[0:1] offset:-3072 nt
	ds_read_b128 v[142:145], v130 offset:45056
	s_waitcnt lgkmcnt(3)
	v_mfma_f32_32x32x16_f16 v[0:15], v[146:149], v[122:125], v[0:15]
	v_add_f32_e32 v29, v135, v29
	global_store_dword v141, v29, s[0:1] offset:-1536 nt
	ds_read_b128 v[146:149], v130 offset:46080
	s_waitcnt lgkmcnt(3)
	v_mfma_f32_32x32x16_f16 v[0:15], v[150:153], v[118:121], v[0:15]
	v_add_f32_e32 v30, v135, v30
	global_store_dword v141, v30, s[0:1] offset:0 nt
	ds_read_b128 v[150:153], v130 offset:47104
	s_waitcnt lgkmcnt(3)
	v_mfma_f32_32x32x16_f16 v[0:15], v[154:157], v[110:113], v[0:15]
	v_add_f32_e32 v31, v135, v31
	global_store_dword v141, v31, s[0:1] offset:1536 nt
	ds_read_b128 v[154:157], v130 offset:48128
	s_waitcnt lgkmcnt(3)
	v_mfma_f32_32x32x16_f16 v[0:15], v[142:145], v[114:117], v[0:15]
	s_waitcnt lgkmcnt(2)
	v_mfma_f32_32x32x16_f16 v[0:15], v[146:149], v[106:109], v[0:15]
	s_waitcnt lgkmcnt(1)
	v_mfma_f32_32x32x16_f16 v[0:15], v[150:153], v[102:105], v[0:15]
	s_waitcnt lgkmcnt(0)
	v_mfma_f32_32x32x16_f16 v[0:15], v[154:157], v[98:101], v[0:15]
	s_nop 7
	s_nop 4
	v_add_f32_e32 v0, v135, v0
	global_store_dword v136, v0, s[2:3] offset:-3072 nt
	v_add_f32_e32 v1, v135, v1
	global_store_dword v136, v1, s[2:3] offset:-1536 nt
	v_add_f32_e32 v2, v135, v2
	global_store_dword v136, v2, s[2:3] offset:0 nt
	v_add_f32_e32 v3, v135, v3
	global_store_dword v136, v3, s[2:3] offset:1536 nt
	v_add_f32_e32 v4, v135, v4
	global_store_dword v137, v4, s[2:3] offset:-3072 nt
	v_add_f32_e32 v5, v135, v5
	global_store_dword v137, v5, s[2:3] offset:-1536 nt
	v_add_f32_e32 v6, v135, v6
	global_store_dword v137, v6, s[2:3] offset:0 nt
	v_add_f32_e32 v7, v135, v7
	global_store_dword v137, v7, s[2:3] offset:1536 nt
	v_add_f32_e32 v8, v135, v8
	global_store_dword v138, v8, s[2:3] offset:-3072 nt
	v_add_f32_e32 v9, v135, v9
	global_store_dword v138, v9, s[2:3] offset:-1536 nt
	v_add_f32_e32 v10, v135, v10
	global_store_dword v138, v10, s[2:3] offset:0 nt
	v_add_f32_e32 v11, v135, v11
	global_store_dword v138, v11, s[2:3] offset:1536 nt
	v_add_f32_e32 v12, v135, v12
	global_store_dword v141, v12, s[2:3] offset:-3072 nt
	v_add_f32_e32 v13, v135, v13
	global_store_dword v141, v13, s[2:3] offset:-1536 nt
	v_add_f32_e32 v14, v135, v14
	global_store_dword v141, v14, s[2:3] offset:0 nt
	v_add_f32_e32 v15, v135, v15
	global_store_dword v141, v15, s[2:3] offset:1536 nt
	s_endpgm
